# v71 + dilated-attention tile loop: compiler-added s_waitcnt vmcnt(0) at the first-half join removed (the counted vmcnt(16) / vmcnt(0) of the two incoming paths already cover it): next tile's loads sta
# baseline (speedup 1.0000x reference)
.LBB0_336:
	v_mfma_f32_32x32x16_bf16 v[50:65], v[126:129], v[66:69], 0
	v_med3_i32 v166, v157, 31, v186
	v_lshl_add_u32 v166, v166, 2, s88
	v_add_u32_e32 v167, 0xffffff84, v166
	v_add_u32_e32 v166, -1, v157
	v_med3_i32 v168, v166, -1, v185
	v_med3_i32 v166, v166, 31, v186
	v_lshl_add_u32 v166, v166, 2, s88
	v_mfma_f32_32x32x16_bf16 v[34:49], v[142:145], v[66:69], 0
	v_add_u32_e32 v192, 0xffffff84, v166
	v_add_u32_e32 v166, -2, v157
	v_lshl_add_u32 v169, v168, 2, s88
	v_med3_i32 v168, v166, -1, v185
	v_med3_i32 v166, v166, 31, v186
	v_lshl_add_u32 v166, v166, 2, s88
	v_add_u32_e32 v194, 0xffffff84, v166
	v_mfma_f32_32x32x16_bf16 v[50:65], v[138:141], v[70:73], v[50:65]
	v_add_u32_e32 v166, -3, v157
	v_med3_i32 v0, v157, -1, v185
	v_lshl_add_u32 v193, v168, 2, s88
	v_med3_i32 v168, v166, -1, v185
	v_med3_i32 v166, v166, 31, v186
	v_lshl_add_u32 v0, v0, 2, s88
	v_lshl_add_u32 v195, v168, 2, s88
	v_mfma_f32_32x32x16_bf16 v[34:49], v[122:125], v[70:73], v[34:49]
	v_lshl_add_u32 v166, v166, 2, s88
	v_add_u32_e32 v196, 0xffffff84, v166
	ds_read_b32 v166, v0 offset:4
	ds_read_b32 v168, v167
	ds_read_b32 v167, v169 offset:4
	ds_read_b32 v169, v192
	ds_read_b32 v192, v193 offset:4
	ds_read_b32 v194, v194
	ds_read_b32 v193, v195 offset:4
	ds_read_b32 v195, v196
	v_add_u32_e32 v0, -8, v157
	v_add_u32_e32 v191, s8, v170
	s_cmp_gt_i32 s8, -1
	v_mfma_f32_32x32x16_bf16 v[50:65], v[118:121], v[74:77], v[50:65]
	v_mfma_f32_32x32x16_bf16 v[34:49], v[134:137], v[74:77], v[34:49]
	v_mfma_f32_32x32x16_bf16 v[50:65], v[130:133], v[78:81], v[50:65]
	v_mfma_f32_32x32x16_bf16 v[34:49], v[114:117], v[78:81], v[34:49]
	s_waitcnt lgkmcnt(0)
	s_nop 9
	v_add_f32_e64 v50, v50, v166
	v_add_f32_e64 v51, v51, v167
	v_pk_add_f32 v[166:167], v[34:35], v[168:169]
	v_pk_add_f32 v[34:35], v[52:53], v[192:193]
	v_add_u32_e32 v53, -9, v157
	v_med3_i32 v168, v53, -1, v185
	v_med3_i32 v53, v53, 31, v186
	v_lshl_add_u32 v53, v53, 2, s88
	v_add_u32_e32 v192, 0xffffff84, v53
	v_add_u32_e32 v53, -10, v157
	v_lshl_add_u32 v169, v168, 2, s88
	v_med3_i32 v168, v53, -1, v185
	v_med3_i32 v53, v53, 31, v186
	v_lshl_add_u32 v53, v53, 2, s88
	v_pk_add_f32 v[36:37], v[36:37], v[194:195]
	v_add_u32_e32 v194, 0xffffff84, v53
	v_add_u32_e32 v53, -11, v157
	v_med3_i32 v52, v0, -1, v185
	v_med3_i32 v0, v0, 31, v186
	v_lshl_add_u32 v193, v168, 2, s88
	v_med3_i32 v168, v53, -1, v185
	v_med3_i32 v53, v53, 31, v186
	v_lshl_add_u32 v52, v52, 2, s88
	v_lshl_add_u32 v0, v0, 2, s88
	v_lshl_add_u32 v195, v168, 2, s88
	v_lshl_add_u32 v53, v53, 2, s88
	v_add_u32_e32 v0, 0xffffff84, v0
	v_add_u32_e32 v196, 0xffffff84, v53
	ds_read_b32 v52, v52 offset:4
	ds_read_b32 v168, v0
	ds_read_b32 v53, v169 offset:4
	ds_read_b32 v169, v192
	ds_read_b32 v192, v193 offset:4
	ds_read_b32 v193, v195 offset:4
	ds_read_b32 v194, v194
	ds_read_b32 v195, v196
	s_waitcnt lgkmcnt(5)
	v_pk_add_f32 v[54:55], v[54:55], v[52:53]
	s_waitcnt lgkmcnt(4)
	v_pk_add_f32 v[52:53], v[38:39], v[168:169]
	s_waitcnt lgkmcnt(2)
	v_pk_add_f32 v[38:39], v[56:57], v[192:193]
	v_subrev_u32_e32 v57, 17, v157
	v_med3_i32 v168, v57, -1, v185
	v_med3_i32 v57, v57, 31, v186
	v_lshl_add_u32 v57, v57, 2, s88
	v_add_u32_e32 v169, 0xffffff84, v57
	v_subrev_u32_e32 v57, 18, v157
	v_med3_i32 v192, v57, -1, v185
	v_med3_i32 v57, v57, 31, v186
	v_lshl_add_u32 v57, v57, 2, s88
	v_add_u32_e32 v0, -16, v157
	v_add_u32_e32 v197, 0xffffff84, v57
	v_subrev_u32_e32 v57, 19, v157
	v_med3_i32 v56, v0, -1, v185
	v_med3_i32 v0, v0, 31, v186
	v_lshl_add_u32 v196, v192, 2, s88
	v_med3_i32 v192, v57, -1, v185
	v_med3_i32 v57, v57, 31, v186
	v_lshl_add_u32 v56, v56, 2, s88
	v_lshl_add_u32 v0, v0, 2, s88
	v_lshl_add_u32 v199, v192, 2, s88
	v_lshl_add_u32 v57, v57, 2, s88
	v_add_u32_e32 v0, 0xffffff84, v0
	v_lshl_add_u32 v168, v168, 2, s88
	v_add_u32_e32 v200, 0xffffff84, v57
	ds_read_b32 v56, v56 offset:4
	ds_read_b32 v192, v0
	ds_read_b32 v57, v168 offset:4
	ds_read_b32 v193, v169
	ds_read_b32 v196, v196 offset:4
	ds_read_b32 v198, v197
	ds_read_b32 v197, v199 offset:4
	ds_read_b32 v199, v200
	s_waitcnt lgkmcnt(5)
	v_pk_add_f32 v[58:59], v[58:59], v[56:57]
	s_waitcnt lgkmcnt(4)
	v_pk_add_f32 v[56:57], v[42:43], v[192:193]
	v_pk_add_f32 v[168:169], v[40:41], v[194:195]
	s_waitcnt lgkmcnt(1)
	v_pk_add_f32 v[40:41], v[60:61], v[196:197]
	s_waitcnt lgkmcnt(0)
	v_pk_add_f32 v[42:43], v[44:45], v[198:199]
	v_subrev_u32_e32 v45, 25, v157
	v_med3_i32 v60, v45, -1, v185
	v_med3_i32 v45, v45, 31, v186
	v_lshl_add_u32 v45, v45, 2, s88
	v_add_u32_e32 v192, 0xffffff84, v45
	v_subrev_u32_e32 v45, 26, v157
	v_lshl_add_u32 v61, v60, 2, s88
	v_med3_i32 v60, v45, -1, v185
	v_med3_i32 v45, v45, 31, v186
	v_lshl_add_u32 v45, v45, 2, s88
	v_subrev_u32_e32 v0, 24, v157
	v_add_u32_e32 v194, 0xffffff84, v45
	v_subrev_u32_e32 v45, 27, v157
	v_med3_i32 v44, v0, -1, v185
	v_med3_i32 v0, v0, 31, v186
	v_lshl_add_u32 v193, v60, 2, s88
	v_med3_i32 v60, v45, -1, v185
	v_med3_i32 v45, v45, 31, v186
	v_lshl_add_u32 v44, v44, 2, s88
	v_lshl_add_u32 v0, v0, 2, s88
	v_lshl_add_u32 v195, v60, 2, s88
	v_lshl_add_u32 v45, v45, 2, s88
	v_add_u32_e32 v0, 0xffffff84, v0
	v_add_u32_e32 v196, 0xffffff84, v45
	ds_read_b32 v44, v44 offset:4
	ds_read_b32 v60, v0
	ds_read_b32 v45, v61 offset:4
	ds_read_b32 v61, v192
	ds_read_b32 v192, v193 offset:4
	ds_read_b32 v193, v195 offset:4
	ds_read_b32 v194, v194
	ds_read_b32 v195, v196
	s_waitcnt lgkmcnt(5)
	v_pk_add_f32 v[62:63], v[62:63], v[44:45]
	s_waitcnt lgkmcnt(4)
	v_pk_add_f32 v[60:61], v[46:47], v[60:61]
	s_waitcnt lgkmcnt(2)
	v_pk_add_f32 v[44:45], v[64:65], v[192:193]
	s_waitcnt lgkmcnt(0)
	v_pk_add_f32 v[46:47], v[48:49], v[194:195]
	s_cbranch_scc1 .LBB0_338
	v_cmp_lt_i32_e32 vcc, -1, v191
	s_nop 1
	v_cndmask_b32_e32 v50, v187, v50, vcc
	v_cmp_lt_i32_e32 vcc, -2, v191
	s_nop 1
	v_cndmask_b32_e32 v51, v187, v51, vcc
	v_cmp_lt_i32_e32 vcc, -3, v191
	s_nop 1
	v_cndmask_b32_e32 v34, v187, v34, vcc
	v_cmp_lt_i32_e32 vcc, -4, v191
	s_nop 1
	v_cndmask_b32_e32 v35, v187, v35, vcc
	v_cmp_lt_i32_e32 vcc, -9, v191
	s_nop 1
	v_cndmask_b32_e32 v54, v187, v54, vcc
	v_cmp_lt_i32_e32 vcc, -10, v191
	s_nop 1
	v_cndmask_b32_e32 v55, v187, v55, vcc
	v_cmp_lt_i32_e32 vcc, -11, v191
	s_nop 1
	v_cndmask_b32_e32 v38, v187, v38, vcc
	v_cmp_lt_i32_e32 vcc, -12, v191
	s_nop 1
	v_cndmask_b32_e32 v39, v187, v39, vcc
	v_cmp_lt_i32_e32 vcc, s53, v191
	s_nop 1
	v_cndmask_b32_e32 v58, v187, v58, vcc
	v_cmp_lt_i32_e32 vcc, s52, v191
	s_nop 1
	v_cndmask_b32_e32 v59, v187, v59, vcc
	v_cmp_lt_i32_e32 vcc, s51, v191
	s_nop 1
	v_cndmask_b32_e32 v40, v187, v40, vcc
	v_cmp_lt_i32_e32 vcc, s50, v191
	s_nop 1
	v_cndmask_b32_e32 v41, v187, v41, vcc
	v_cmp_lt_i32_e32 vcc, s49, v191
	s_nop 1
	v_cndmask_b32_e32 v62, v187, v62, vcc
	v_cmp_lt_i32_e32 vcc, s48, v191
	s_nop 1
	v_cndmask_b32_e32 v63, v187, v63, vcc
	v_cmp_lt_i32_e32 vcc, s47, v191
	s_nop 1
	v_cndmask_b32_e32 v44, v187, v44, vcc
	v_cmp_lt_i32_e32 vcc, s46, v191
	s_nop 1
	v_cndmask_b32_e32 v45, v187, v45, vcc
	v_cmp_lt_i32_e32 vcc, s70, v191
	s_nop 1
	v_cndmask_b32_e32 v166, v187, v166, vcc
	v_cmp_lt_i32_e32 vcc, s69, v191
	s_nop 1
	v_cndmask_b32_e32 v167, v187, v167, vcc
	v_cmp_lt_i32_e32 vcc, s68, v191
	s_nop 1
	v_cndmask_b32_e32 v36, v187, v36, vcc
	v_cmp_lt_i32_e32 vcc, s67, v191
	s_nop 1
	v_cndmask_b32_e32 v37, v187, v37, vcc
	v_cmp_lt_i32_e32 vcc, s66, v191
	s_nop 1
	v_cndmask_b32_e32 v52, v187, v52, vcc
	v_cmp_lt_i32_e32 vcc, s65, v191
	s_nop 1
	v_cndmask_b32_e32 v53, v187, v53, vcc
	v_cmp_lt_i32_e32 vcc, s64, v191
	s_nop 1
	v_cndmask_b32_e32 v168, v187, v168, vcc
	v_cmp_lt_i32_e32 vcc, s63, v191
	s_nop 1
	v_cndmask_b32_e32 v169, v187, v169, vcc
	v_cmp_lt_i32_e32 vcc, s62, v191
	s_nop 1
	v_cndmask_b32_e32 v56, v187, v56, vcc
	v_cmp_lt_i32_e32 vcc, s61, v191
	s_nop 1
	v_cndmask_b32_e32 v57, v187, v57, vcc
	v_cmp_lt_i32_e32 vcc, s60, v191
	s_nop 1
	v_cndmask_b32_e32 v42, v187, v42, vcc
	v_cmp_lt_i32_e32 vcc, s59, v191
	s_nop 1
	v_cndmask_b32_e32 v43, v187, v43, vcc
	v_cmp_lt_i32_e32 vcc, s58, v191
	s_nop 1
	v_cndmask_b32_e32 v60, v187, v60, vcc
	v_cmp_lt_i32_e32 vcc, s57, v191
	s_nop 1
	v_cndmask_b32_e32 v61, v187, v61, vcc
	v_cmp_lt_i32_e32 vcc, s56, v191
	s_nop 1
	v_cndmask_b32_e32 v46, v187, v46, vcc
	v_cmp_lt_i32_e32 vcc, s55, v191
	s_nop 1
	v_cndmask_b32_e32 v47, v187, v47, vcc
